# v049 + non-temporal hint on the 24 converted-weight stores of phase 0
# speedup vs baseline: 1.0161x; 1.0018x over previous
.LBB0_23:
	s_waitcnt lgkmcnt(7)
	v_mul_f32_e32 v80, 0x42800000, v80
	v_med3_f32 v88, v80, s20, v171
	v_mul_f32_e32 v80, 0x42800000, v81
	v_med3_f32 v81, v80, s20, v171
	v_mov_b32_e32 v80, v137
	v_cvt_pk_fp8_f32 v80, v88, v81
	s_waitcnt lgkmcnt(6)
	v_mul_f32_e32 v82, 0x42800000, v82
	v_mul_f32_e32 v83, 0x42800000, v83
	v_med3_f32 v82, v82, s20, v171
	v_med3_f32 v83, v83, s20, v171
	s_waitcnt lgkmcnt(1)
	v_mul_f32_e32 v68, 0x42800000, v68
	v_mul_f32_e32 v69, 0x42800000, v69
	v_cvt_pk_fp8_f32 v80, v82, v83 op_sel:[0,0,1]
	v_mul_f32_e32 v76, 0x42800000, v76
	v_mul_f32_e32 v77, 0x42800000, v77
	v_mul_f32_e32 v72, 0x42800000, v72
	v_mul_f32_e32 v73, 0x42800000, v73
	v_med3_f32 v68, v68, s20, v171
	v_med3_f32 v69, v69, s20, v171
	v_mov_b32_e32 v83, v137
	v_med3_f32 v76, v76, s20, v171
	v_med3_f32 v77, v77, s20, v171
	v_mov_b32_e32 v81, v137
	v_med3_f32 v72, v72, s20, v171
	v_med3_f32 v73, v73, s20, v171
	v_mov_b32_e32 v82, v137
	v_cvt_pk_fp8_f32 v83, v68, v69
	v_cvt_pk_fp8_f32 v81, v76, v77
	v_cvt_pk_fp8_f32 v82, v72, v73
	s_waitcnt lgkmcnt(0)
	v_mul_f32_e32 v70, 0x42800000, v70
	v_mul_f32_e32 v71, 0x42800000, v71
	v_mul_f32_e32 v78, 0x42800000, v78
	v_mul_f32_e32 v79, 0x42800000, v79
	v_mul_f32_e32 v74, 0x42800000, v74
	v_mul_f32_e32 v75, 0x42800000, v75
	v_med3_f32 v70, v70, s20, v171
	v_med3_f32 v71, v71, s20, v171
	v_ashrrev_i32_e32 v68, 8, v86
	v_med3_f32 v78, v78, s20, v171
	v_med3_f32 v79, v79, s20, v171
	v_med3_f32 v74, v74, s20, v171
	v_med3_f32 v75, v75, s20, v171
	v_cvt_pk_fp8_f32 v83, v70, v71 op_sel:[0,0,1]
	v_mad_i64_i32 v[66:67], s[0:1], s2, v68, v[66:67]
	v_lshrrev_b32_e32 v70, 3, v87
	v_cvt_pk_fp8_f32 v81, v78, v79 op_sel:[0,0,1]
	v_cvt_pk_fp8_f32 v82, v74, v75 op_sel:[0,0,1]
	v_lshlrev_b64 v[66:67], 15, v[66:67]
	v_lshlrev_b32_e32 v68, 7, v86
	v_and_or_b32 v70, v70, s12, v84
	v_lshlrev_b32_e32 v71, 6, v87
	v_lshlrev_b32_e32 v72, 2, v87
	v_and_b32_e32 v68, 0x4000, v68
	v_mov_b32_e32 v69, v137
	v_and_or_b32 v71, v71, s13, v85
	v_lshlrev_b32_e32 v70, 10, v70
	v_and_b32_e32 v72, 32, v72
	v_lshl_add_u64 v[66:67], s[70:71], 0, v[66:67]
	v_bitop3_b32 v70, v71, v70, v72 bitop3:0xde
	v_mov_b32_e32 v71, v137
	v_lshl_add_u64 v[66:67], v[66:67], 0, v[68:69]
	v_lshl_add_u64 v[66:67], v[66:67], 0, v[70:71]
	global_store_dwordx4 v[66:67], v[80:83], off nt
	s_waitcnt lgkmcnt(0)

.LBB0_30:
	s_ashr_i32 s0, s4, 31
	v_add_u32_e32 v143, s35, v154
	s_lshr_b32 s0, s0, 26
	s_add_i32 s0, s4, s0
	v_ashrrev_i32_e32 v138, 6, v143
	s_ashr_i32 s2, s0, 6
	v_ashrrev_i32_e32 v140, 8, v177
	v_ashrrev_i32_e32 v139, 31, v138
	v_mad_i64_i32 v[140:141], s[0:1], s2, v140, v[138:139]
	v_lshlrev_b64 v[144:145], 15, v[140:141]
	v_lshlrev_b32_e32 v140, 7, v177
	v_and_b32_e32 v146, 0x4000, v140
	v_lshrrev_b32_e32 v141, 3, v142
	v_bfe_u32 v140, v143, 5, 1
	v_and_or_b32 v148, v141, s12, v140
	v_lshlrev_b32_e32 v141, 1, v143
	v_lshlrev_b32_e32 v149, 6, v142
	v_and_b32_e32 v141, 62, v141
	v_lshlrev_b32_e32 v142, 2, v142
	v_mov_b32_e32 v147, v137
	v_and_or_b32 v143, v149, s13, v141
	v_lshlrev_b32_e32 v148, 10, v148
	v_and_b32_e32 v142, 32, v142
	v_lshl_add_u64 v[144:145], s[70:71], 0, v[144:145]
	v_bitop3_b32 v142, v143, v148, v142 bitop3:0xde
	v_mov_b32_e32 v143, v137
	v_lshl_add_u64 v[144:145], v[144:145], 0, v[146:147]
	v_lshl_add_u64 v[142:143], v[144:145], 0, v[142:143]
	global_store_dwordx4 v[142:143], v[130:133], off nt
	ds_read2_b32 v[130:131], v155 offset0:8 offset1:73
	ds_read2_b32 v[132:133], v155 offset0:138 offset1:203
	s_waitcnt lgkmcnt(1)
	v_cvt_pk_bf16_f32 v130, v130, v131
	s_waitcnt lgkmcnt(0)
	v_cvt_pk_bf16_f32 v131, v132, v133
	ds_read2_b32 v[132:133], v172 offset0:12 offset1:77
	ds_read2_b32 v[142:143], v172 offset0:142 offset1:207
	s_waitcnt lgkmcnt(1)
	v_cvt_pk_bf16_f32 v132, v132, v133
	s_waitcnt lgkmcnt(0)
	v_cvt_pk_bf16_f32 v133, v142, v143
	v_cndmask_b32_e64 v143, 0, 1, s[90:91]
	v_add_u32_e32 v142, s15, v156
	s_mov_b64 s[96:97], -1
	v_cmp_ne_u32_e64 s[0:1], 1, v143
	s_andn2_b64 vcc, exec, s[90:91]
	s_cbranch_vccnz .LBB0_32
	v_and_b32_e32 v143, 0x7f, v142
	s_mov_b64 s[96:97], 0

.LBB0_34:
	v_ashrrev_i32_e32 v144, 8, v142
	v_lshlrev_b32_e32 v142, 7, v142
	v_mad_i64_i32 v[144:145], s[26:27], s2, v144, v[138:139]
	v_and_b32_e32 v146, 0x4000, v142
	v_lshrrev_b32_e32 v142, 3, v143
	v_lshlrev_b64 v[144:145], 15, v[144:145]
	v_and_or_b32 v142, v142, s12, v140
	v_lshlrev_b32_e32 v148, 6, v143
	v_lshlrev_b32_e32 v143, 2, v143
	v_mov_b32_e32 v147, v137
	v_and_or_b32 v148, v148, s13, v141
	v_lshlrev_b32_e32 v142, 10, v142
	v_and_b32_e32 v143, 32, v143
	v_lshl_add_u64 v[144:145], s[70:71], 0, v[144:145]
	v_bitop3_b32 v142, v148, v142, v143 bitop3:0xde
	v_mov_b32_e32 v143, v137
	v_lshl_add_u64 v[144:145], v[144:145], 0, v[146:147]
	v_lshl_add_u64 v[142:143], v[144:145], 0, v[142:143]
	global_store_dwordx4 v[142:143], v[130:133], off nt
	ds_read2_b32 v[130:131], v155 offset0:16 offset1:81
	ds_read2_b32 v[132:133], v155 offset0:146 offset1:211
	s_waitcnt lgkmcnt(1)
	v_cvt_pk_bf16_f32 v130, v130, v131
	s_waitcnt lgkmcnt(0)
	v_cvt_pk_bf16_f32 v131, v132, v133
	ds_read2_b32 v[132:133], v172 offset0:20 offset1:85
	ds_read2_b32 v[142:143], v172 offset0:150 offset1:215
	s_waitcnt lgkmcnt(1)
	v_cvt_pk_bf16_f32 v132, v132, v133
	s_waitcnt lgkmcnt(0)
	v_cvt_pk_bf16_f32 v133, v142, v143
	v_add_u32_e32 v142, s15, v157
	s_mov_b64 s[96:97], -1
	s_and_b64 vcc, exec, s[0:1]
	s_cbranch_vccnz .LBB0_36
	v_and_b32_e32 v143, 0x7f, v142
	s_mov_b64 s[96:97], 0

.LBB0_38:
	v_ashrrev_i32_e32 v144, 8, v142
	v_lshlrev_b32_e32 v142, 7, v142
	v_mad_i64_i32 v[144:145], s[26:27], s2, v144, v[138:139]
	v_and_b32_e32 v146, 0x4000, v142
	v_lshrrev_b32_e32 v142, 3, v143
	v_lshlrev_b64 v[144:145], 15, v[144:145]
	v_and_or_b32 v142, v142, s12, v140
	v_lshlrev_b32_e32 v148, 6, v143
	v_lshlrev_b32_e32 v143, 2, v143
	v_mov_b32_e32 v147, v137
	v_and_or_b32 v148, v148, s13, v141
	v_lshlrev_b32_e32 v142, 10, v142
	v_and_b32_e32 v143, 32, v143
	v_lshl_add_u64 v[144:145], s[70:71], 0, v[144:145]
	v_bitop3_b32 v142, v148, v142, v143 bitop3:0xde
	v_mov_b32_e32 v143, v137
	v_lshl_add_u64 v[144:145], v[144:145], 0, v[146:147]
	v_lshl_add_u64 v[142:143], v[144:145], 0, v[142:143]
	global_store_dwordx4 v[142:143], v[130:133], off nt
	ds_read2_b32 v[130:131], v155 offset0:24 offset1:89
	ds_read2_b32 v[132:133], v155 offset0:154 offset1:219
	s_waitcnt lgkmcnt(1)
	v_cvt_pk_bf16_f32 v130, v130, v131
	s_waitcnt lgkmcnt(0)
	v_cvt_pk_bf16_f32 v131, v132, v133
	ds_read2_b32 v[132:133], v172 offset0:28 offset1:93
	ds_read2_b32 v[142:143], v172 offset0:158 offset1:223
	s_waitcnt lgkmcnt(1)
	v_cvt_pk_bf16_f32 v132, v132, v133
	s_waitcnt lgkmcnt(0)
	v_cvt_pk_bf16_f32 v133, v142, v143
	v_add_u32_e32 v142, s15, v158
	s_mov_b64 s[96:97], -1
	s_and_b64 vcc, exec, s[0:1]
	s_cbranch_vccnz .LBB0_40
	v_and_b32_e32 v143, 0x7f, v142
	s_mov_b64 s[96:97], 0

.LBB0_42:
	v_ashrrev_i32_e32 v144, 8, v142
	v_lshlrev_b32_e32 v142, 7, v142
	v_mad_i64_i32 v[144:145], s[26:27], s2, v144, v[138:139]
	v_and_b32_e32 v146, 0x4000, v142
	v_lshrrev_b32_e32 v142, 3, v143
	v_lshlrev_b64 v[144:145], 15, v[144:145]
	v_and_or_b32 v142, v142, s12, v140
	v_lshlrev_b32_e32 v148, 6, v143
	v_lshlrev_b32_e32 v143, 2, v143
	v_mov_b32_e32 v147, v137
	v_and_or_b32 v148, v148, s13, v141
	v_lshlrev_b32_e32 v142, 10, v142
	v_and_b32_e32 v143, 32, v143
	v_lshl_add_u64 v[144:145], s[70:71], 0, v[144:145]
	v_bitop3_b32 v142, v148, v142, v143 bitop3:0xde
	v_mov_b32_e32 v143, v137
	v_lshl_add_u64 v[144:145], v[144:145], 0, v[146:147]
	v_lshl_add_u64 v[142:143], v[144:145], 0, v[142:143]
	global_store_dwordx4 v[142:143], v[130:133], off nt
	ds_read2_b32 v[130:131], v155 offset0:32 offset1:97
	ds_read2_b32 v[132:133], v155 offset0:162 offset1:227
	s_waitcnt lgkmcnt(1)
	v_cvt_pk_bf16_f32 v130, v130, v131
	s_waitcnt lgkmcnt(0)
	v_cvt_pk_bf16_f32 v131, v132, v133
	ds_read2_b32 v[132:133], v172 offset0:36 offset1:101
	ds_read2_b32 v[142:143], v172 offset0:166 offset1:231
	s_waitcnt lgkmcnt(1)
	v_cvt_pk_bf16_f32 v132, v132, v133
	s_waitcnt lgkmcnt(0)
	v_cvt_pk_bf16_f32 v133, v142, v143
	v_add_u32_e32 v142, s15, v159
	s_mov_b64 s[96:97], -1
	s_and_b64 vcc, exec, s[0:1]
	s_cbranch_vccnz .LBB0_44
	v_and_b32_e32 v143, 0x7f, v142
	s_mov_b64 s[96:97], 0

.LBB0_46:
	v_ashrrev_i32_e32 v144, 8, v142
	v_lshlrev_b32_e32 v142, 7, v142
	v_mad_i64_i32 v[144:145], s[26:27], s2, v144, v[138:139]
	v_and_b32_e32 v146, 0x4000, v142
	v_lshrrev_b32_e32 v142, 3, v143
	v_lshlrev_b64 v[144:145], 15, v[144:145]
	v_and_or_b32 v142, v142, s12, v140
	v_lshlrev_b32_e32 v148, 6, v143
	v_lshlrev_b32_e32 v143, 2, v143
	v_mov_b32_e32 v147, v137
	v_and_or_b32 v148, v148, s13, v141
	v_lshlrev_b32_e32 v142, 10, v142
	v_and_b32_e32 v143, 32, v143
	v_lshl_add_u64 v[144:145], s[70:71], 0, v[144:145]
	v_bitop3_b32 v142, v148, v142, v143 bitop3:0xde
	v_mov_b32_e32 v143, v137
	v_lshl_add_u64 v[144:145], v[144:145], 0, v[146:147]
	v_lshl_add_u64 v[142:143], v[144:145], 0, v[142:143]
	global_store_dwordx4 v[142:143], v[130:133], off nt
	ds_read2_b32 v[130:131], v155 offset0:40 offset1:105
	ds_read2_b32 v[132:133], v155 offset0:170 offset1:235
	s_waitcnt lgkmcnt(1)
	v_cvt_pk_bf16_f32 v130, v130, v131
	s_waitcnt lgkmcnt(0)
	v_cvt_pk_bf16_f32 v131, v132, v133
	ds_read2_b32 v[132:133], v172 offset0:44 offset1:109
	ds_read2_b32 v[142:143], v172 offset0:174 offset1:239
	s_waitcnt lgkmcnt(1)
	v_cvt_pk_bf16_f32 v132, v132, v133
	s_waitcnt lgkmcnt(0)
	v_cvt_pk_bf16_f32 v133, v142, v143
	v_add_u32_e32 v142, s15, v160
	s_mov_b64 s[96:97], -1
	s_and_b64 vcc, exec, s[0:1]
	s_cbranch_vccnz .LBB0_48
	v_and_b32_e32 v143, 0x7f, v142
	s_mov_b64 s[96:97], 0

.LBB0_50:
	v_ashrrev_i32_e32 v144, 8, v142
	v_lshlrev_b32_e32 v142, 7, v142
	v_mad_i64_i32 v[144:145], s[26:27], s2, v144, v[138:139]
	v_and_b32_e32 v146, 0x4000, v142
	v_lshrrev_b32_e32 v142, 3, v143
	v_lshlrev_b64 v[144:145], 15, v[144:145]
	v_and_or_b32 v142, v142, s12, v140
	v_lshlrev_b32_e32 v148, 6, v143
	v_lshlrev_b32_e32 v143, 2, v143
	v_mov_b32_e32 v147, v137
	v_and_or_b32 v148, v148, s13, v141
	v_lshlrev_b32_e32 v142, 10, v142
	v_and_b32_e32 v143, 32, v143
	v_lshl_add_u64 v[144:145], s[70:71], 0, v[144:145]
	v_bitop3_b32 v142, v148, v142, v143 bitop3:0xde
	v_mov_b32_e32 v143, v137
	v_lshl_add_u64 v[144:145], v[144:145], 0, v[146:147]
	v_lshl_add_u64 v[142:143], v[144:145], 0, v[142:143]
	global_store_dwordx4 v[142:143], v[130:133], off nt
	ds_read2_b32 v[130:131], v155 offset0:48 offset1:113
	ds_read2_b32 v[132:133], v155 offset0:178 offset1:243
	s_waitcnt lgkmcnt(1)
	v_cvt_pk_bf16_f32 v130, v130, v131
	s_waitcnt lgkmcnt(0)
	v_cvt_pk_bf16_f32 v131, v132, v133
	ds_read2_b32 v[132:133], v172 offset0:52 offset1:117
	ds_read2_b32 v[142:143], v172 offset0:182 offset1:247
	s_waitcnt lgkmcnt(1)
	v_cvt_pk_bf16_f32 v132, v132, v133
	s_waitcnt lgkmcnt(0)
	v_cvt_pk_bf16_f32 v133, v142, v143
	v_add_u32_e32 v142, s15, v161
	s_mov_b64 s[96:97], -1
	s_and_b64 vcc, exec, s[0:1]
	s_cbranch_vccnz .LBB0_52
	v_and_b32_e32 v143, 0x7f, v142
	s_mov_b64 s[96:97], 0

.LBB0_54:
	v_ashrrev_i32_e32 v144, 8, v142
	v_lshlrev_b32_e32 v142, 7, v142
	v_mad_i64_i32 v[144:145], s[26:27], s2, v144, v[138:139]
	v_and_b32_e32 v146, 0x4000, v142
	v_lshrrev_b32_e32 v142, 3, v143
	v_lshlrev_b64 v[144:145], 15, v[144:145]
	v_and_or_b32 v142, v142, s12, v140
	v_lshlrev_b32_e32 v148, 6, v143
	v_lshlrev_b32_e32 v143, 2, v143
	v_mov_b32_e32 v147, v137
	v_and_or_b32 v148, v148, s13, v141
	v_lshlrev_b32_e32 v142, 10, v142
	v_and_b32_e32 v143, 32, v143
	v_lshl_add_u64 v[144:145], s[70:71], 0, v[144:145]
	v_bitop3_b32 v142, v148, v142, v143 bitop3:0xde
	v_mov_b32_e32 v143, v137
	v_lshl_add_u64 v[144:145], v[144:145], 0, v[146:147]
	v_lshl_add_u64 v[142:143], v[144:145], 0, v[142:143]
	global_store_dwordx4 v[142:143], v[130:133], off nt
	ds_read2_b32 v[130:131], v155 offset0:56 offset1:121
	ds_read2_b32 v[132:133], v155 offset0:186 offset1:251
	s_waitcnt lgkmcnt(1)
	v_cvt_pk_bf16_f32 v130, v130, v131
	s_waitcnt lgkmcnt(0)
	v_cvt_pk_bf16_f32 v131, v132, v133
	ds_read2_b32 v[132:133], v172 offset0:60 offset1:125
	ds_read2_b32 v[142:143], v172 offset0:190 offset1:255
	s_waitcnt lgkmcnt(1)
	v_cvt_pk_bf16_f32 v132, v132, v133
	s_waitcnt lgkmcnt(0)
	v_cvt_pk_bf16_f32 v133, v142, v143
	v_add_u32_e32 v142, s15, v162
	s_mov_b64 s[96:97], -1
	s_and_b64 vcc, exec, s[0:1]
	s_cbranch_vccnz .LBB0_56
	v_and_b32_e32 v143, 0x7f, v142
	s_mov_b64 s[96:97], 0

.LBB0_58:
	v_ashrrev_i32_e32 v144, 8, v142
	v_lshlrev_b32_e32 v142, 7, v142
	v_mad_i64_i32 v[138:139], s[0:1], s2, v144, v[138:139]
	v_and_b32_e32 v144, 0x4000, v142
	v_lshrrev_b32_e32 v142, 3, v143
	v_and_or_b32 v140, v142, s12, v140
	v_lshlrev_b32_e32 v142, 6, v143
	v_lshlrev_b64 v[138:139], 15, v[138:139]
	v_and_or_b32 v141, v142, s13, v141
	v_lshlrev_b32_e32 v142, 2, v143
	v_mov_b32_e32 v145, v137
	v_lshlrev_b32_e32 v140, 10, v140
	v_and_b32_e32 v142, 32, v142
	v_lshl_add_u64 v[138:139], s[70:71], 0, v[138:139]
	v_bitop3_b32 v140, v141, v140, v142 bitop3:0xde
	v_mov_b32_e32 v141, v137
	v_lshl_add_u64 v[138:139], v[138:139], 0, v[144:145]
	v_lshl_add_u64 v[138:139], v[138:139], 0, v[140:141]
	global_store_dwordx4 v[138:139], v[130:133], off nt
	s_waitcnt lgkmcnt(0)
	s_mov_b64 s[0:1], 0

.LBB0_64:
	s_waitcnt lgkmcnt(7)
	v_mul_f32_e32 v148, 0x42800000, v148
	v_mul_f32_e32 v149, 0x42800000, v149
	s_waitcnt lgkmcnt(6)
	v_mul_f32_e32 v151, 0x42800000, v146
	v_med3_f32 v148, v148, s20, v171
	v_med3_f32 v149, v149, s20, v171
	v_mov_b32_e32 v146, v137
	v_cvt_pk_fp8_f32 v146, v148, v149
	s_waitcnt lgkmcnt(1)
	v_mul_f32_e32 v132, 0x42800000, v132
	v_mul_f32_e32 v133, 0x42800000, v133
	v_mul_f32_e32 v147, 0x42800000, v147
	v_med3_f32 v132, v132, s20, v171
	v_med3_f32 v133, v133, s20, v171
	v_mov_b32_e32 v149, v137
	v_med3_f32 v148, v151, s20, v171
	v_med3_f32 v147, v147, s20, v171
	v_mul_f32_e32 v144, 0x42800000, v144
	v_mul_f32_e32 v145, 0x42800000, v145
	v_cvt_pk_fp8_f32 v149, v132, v133
	v_cvt_pk_fp8_f32 v146, v148, v147 op_sel:[0,0,1]
	v_med3_f32 v144, v144, s20, v171
	v_med3_f32 v145, v145, s20, v171
	v_mov_b32_e32 v147, v137
	v_mul_f32_e32 v140, 0x42800000, v140
	v_mul_f32_e32 v141, 0x42800000, v141
	v_cvt_pk_fp8_f32 v147, v144, v145
	v_med3_f32 v140, v140, s20, v171
	v_med3_f32 v141, v141, s20, v171
	v_mov_b32_e32 v148, v137
	s_waitcnt lgkmcnt(0)
	v_mul_f32_e32 v130, 0x42800000, v130
	v_mul_f32_e32 v131, 0x42800000, v131
	s_ashr_i32 s0, s4, 31
	v_cvt_pk_fp8_f32 v148, v140, v141
	v_med3_f32 v130, v130, s20, v171
	v_med3_f32 v131, v131, s20, v171
	v_add_u32_e32 v140, s35, v163
	s_lshr_b32 s0, s0, 25
	v_mul_f32_e32 v142, 0x42800000, v142
	v_mul_f32_e32 v143, 0x42800000, v143
	v_cvt_pk_fp8_f32 v149, v130, v131 op_sel:[0,0,1]
	s_add_i32 s0, s4, s0
	v_ashrrev_i32_e32 v130, 7, v140
	v_med3_f32 v142, v142, s20, v171
	v_med3_f32 v143, v143, s20, v171
	v_mul_f32_e32 v138, 0x42800000, v138
	v_mul_f32_e32 v139, 0x42800000, v139
	s_ashr_i32 s2, s0, 7
	v_ashrrev_i32_e32 v132, 8, v176
	v_ashrrev_i32_e32 v131, 31, v130
	v_cvt_pk_fp8_f32 v147, v142, v143 op_sel:[0,0,1]
	v_med3_f32 v138, v138, s20, v171
	v_med3_f32 v139, v139, s20, v171
	v_mad_i64_i32 v[132:133], s[0:1], s2, v132, v[130:131]
	v_lshrrev_b32_e32 v141, 3, v150
	v_bfe_u32 v208, v140, 6, 1
	v_lshlrev_b32_e32 v142, 6, v150
	v_and_b32_e32 v209, 62, v140
	v_cvt_pk_fp8_f32 v148, v138, v139 op_sel:[0,0,1]
	v_lshlrev_b64 v[132:133], 15, v[132:133]
	v_lshlrev_b32_e32 v138, 7, v176
	v_and_or_b32 v141, v141, s12, v208
	v_and_or_b32 v140, v142, s13, v209
	v_lshlrev_b32_e32 v142, 2, v150
	v_and_b32_e32 v138, 0x4000, v138
	v_mov_b32_e32 v139, v137
	v_lshlrev_b32_e32 v141, 10, v141
	v_and_b32_e32 v142, 32, v142
	v_lshl_add_u64 v[132:133], s[70:71], 0, v[132:133]
	v_bitop3_b32 v140, v140, v141, v142 bitop3:0xde
	v_mov_b32_e32 v141, v137
	v_lshl_add_u64 v[132:133], v[132:133], 0, v[138:139]
	v_lshl_add_u64 v[132:133], v[132:133], 0, v[140:141]
	global_store_dwordx4 v[132:133], v[146:149], off nt
	ds_read2_b32 v[150:151], v164 offset0:16 offset1:81
	ds_read2_b32 v[148:149], v164 offset0:146 offset1:211
	ds_read2_b32 v[146:147], v175 offset0:20 offset1:85
	ds_read2_b32 v[144:145], v175 offset0:150 offset1:215
	ds_read2_b32 v[142:143], v174 offset0:24 offset1:89
	ds_read2_b32 v[140:141], v174 offset0:154 offset1:219
	ds_read2_b32 v[138:139], v173 offset0:28 offset1:93
	ds_read2_b32 v[132:133], v173 offset0:158 offset1:223
	v_cndmask_b32_e64 v211, 0, 1, s[90:91]
	v_add_u32_e32 v210, s15, v165
	v_cmp_ne_u32_e64 s[0:1], 1, v211
	s_andn2_b64 vcc, exec, s[90:91]
	s_mov_b64 s[96:97], -1
	s_cbranch_vccnz .LBB0_66
	v_and_b32_e32 v211, 0x7f, v210
	s_mov_b64 s[96:97], 0

.LBB0_68:
	s_waitcnt lgkmcnt(7)
	v_mul_f32_e32 v150, 0x42800000, v150
	v_mul_f32_e32 v151, 0x42800000, v151
	s_waitcnt lgkmcnt(6)
	v_mul_f32_e32 v212, 0x42800000, v148
	v_med3_f32 v150, v150, s20, v171
	v_med3_f32 v151, v151, s20, v171
	v_mov_b32_e32 v148, v137
	v_cvt_pk_fp8_f32 v148, v150, v151
	v_mul_f32_e32 v149, 0x42800000, v149
	s_waitcnt lgkmcnt(1)
	v_mul_f32_e32 v138, 0x42800000, v138
	v_mul_f32_e32 v139, 0x42800000, v139
	v_med3_f32 v150, v212, s20, v171
	v_med3_f32 v149, v149, s20, v171
	v_mul_f32_e32 v142, 0x42800000, v142
	v_mul_f32_e32 v143, 0x42800000, v143
	v_med3_f32 v138, v138, s20, v171
	v_med3_f32 v139, v139, s20, v171
	v_mov_b32_e32 v151, v137
	v_cvt_pk_fp8_f32 v148, v150, v149 op_sel:[0,0,1]
	v_mul_f32_e32 v146, 0x42800000, v146
	v_mul_f32_e32 v147, 0x42800000, v147
	v_med3_f32 v142, v142, s20, v171
	v_med3_f32 v143, v143, s20, v171
	v_mov_b32_e32 v150, v137
	v_cvt_pk_fp8_f32 v151, v138, v139
	v_med3_f32 v146, v146, s20, v171
	v_med3_f32 v147, v147, s20, v171
	v_mov_b32_e32 v149, v137
	v_cvt_pk_fp8_f32 v150, v142, v143
	v_cvt_pk_fp8_f32 v149, v146, v147
	s_waitcnt lgkmcnt(0)
	v_mul_f32_e32 v132, 0x42800000, v132
	v_mul_f32_e32 v133, 0x42800000, v133
	v_mul_f32_e32 v140, 0x42800000, v140
	v_mul_f32_e32 v141, 0x42800000, v141
	v_med3_f32 v132, v132, s20, v171
	v_med3_f32 v133, v133, s20, v171
	v_mul_f32_e32 v144, 0x42800000, v144
	v_mul_f32_e32 v145, 0x42800000, v145
	v_med3_f32 v140, v140, s20, v171
	v_med3_f32 v141, v141, s20, v171
	v_cvt_pk_fp8_f32 v151, v132, v133 op_sel:[0,0,1]
	v_ashrrev_i32_e32 v132, 8, v210
	v_med3_f32 v144, v144, s20, v171
	v_med3_f32 v145, v145, s20, v171
	v_cvt_pk_fp8_f32 v150, v140, v141 op_sel:[0,0,1]
	v_mad_i64_i32 v[132:133], s[26:27], s2, v132, v[130:131]
	v_lshrrev_b32_e32 v140, 3, v211
	v_cvt_pk_fp8_f32 v149, v144, v145 op_sel:[0,0,1]
	v_lshlrev_b64 v[132:133], 15, v[132:133]
	v_lshlrev_b32_e32 v138, 7, v210
	v_and_or_b32 v140, v140, s12, v208
	v_lshlrev_b32_e32 v141, 6, v211
	v_lshlrev_b32_e32 v142, 2, v211
	v_and_b32_e32 v138, 0x4000, v138
	v_mov_b32_e32 v139, v137
	v_and_or_b32 v141, v141, s13, v209
	v_lshlrev_b32_e32 v140, 10, v140
	v_and_b32_e32 v142, 32, v142
	v_lshl_add_u64 v[132:133], s[70:71], 0, v[132:133]
	v_bitop3_b32 v140, v141, v140, v142 bitop3:0xde
	v_mov_b32_e32 v141, v137
	v_lshl_add_u64 v[132:133], v[132:133], 0, v[138:139]
	v_lshl_add_u64 v[132:133], v[132:133], 0, v[140:141]
	global_store_dwordx4 v[132:133], v[148:151], off nt
	ds_read2_b32 v[150:151], v164 offset0:32 offset1:97
	ds_read2_b32 v[148:149], v164 offset0:162 offset1:227
	ds_read2_b32 v[146:147], v175 offset0:36 offset1:101
	ds_read2_b32 v[144:145], v175 offset0:166 offset1:231
	ds_read2_b32 v[142:143], v174 offset0:40 offset1:105
	ds_read2_b32 v[140:141], v174 offset0:170 offset1:235
	ds_read2_b32 v[138:139], v173 offset0:44 offset1:109
	ds_read2_b32 v[132:133], v173 offset0:174 offset1:239
	v_add_u32_e32 v210, s15, v166
	s_mov_b64 s[96:97], -1
	s_and_b64 vcc, exec, s[0:1]
	s_cbranch_vccnz .LBB0_70
	v_and_b32_e32 v211, 0x7f, v210
	s_mov_b64 s[96:97], 0

.LBB0_72:
	s_waitcnt lgkmcnt(7)
	v_mul_f32_e32 v150, 0x42800000, v150
	v_mul_f32_e32 v151, 0x42800000, v151
	s_waitcnt lgkmcnt(6)
	v_mul_f32_e32 v212, 0x42800000, v148
	v_med3_f32 v150, v150, s20, v171
	v_med3_f32 v151, v151, s20, v171
	v_mov_b32_e32 v148, v137
	v_cvt_pk_fp8_f32 v148, v150, v151
	v_mul_f32_e32 v149, 0x42800000, v149
	s_waitcnt lgkmcnt(1)
	v_mul_f32_e32 v138, 0x42800000, v138
	v_mul_f32_e32 v139, 0x42800000, v139
	v_med3_f32 v150, v212, s20, v171
	v_med3_f32 v149, v149, s20, v171
	v_mul_f32_e32 v142, 0x42800000, v142
	v_mul_f32_e32 v143, 0x42800000, v143
	v_med3_f32 v138, v138, s20, v171
	v_med3_f32 v139, v139, s20, v171
	v_mov_b32_e32 v151, v137
	v_cvt_pk_fp8_f32 v148, v150, v149 op_sel:[0,0,1]
	v_mul_f32_e32 v146, 0x42800000, v146
	v_mul_f32_e32 v147, 0x42800000, v147
	v_med3_f32 v142, v142, s20, v171
	v_med3_f32 v143, v143, s20, v171
	v_mov_b32_e32 v150, v137
	v_cvt_pk_fp8_f32 v151, v138, v139
	v_med3_f32 v146, v146, s20, v171
	v_med3_f32 v147, v147, s20, v171
	v_mov_b32_e32 v149, v137
	v_cvt_pk_fp8_f32 v150, v142, v143
	v_cvt_pk_fp8_f32 v149, v146, v147
	s_waitcnt lgkmcnt(0)
	v_mul_f32_e32 v132, 0x42800000, v132
	v_mul_f32_e32 v133, 0x42800000, v133
	v_mul_f32_e32 v140, 0x42800000, v140
	v_mul_f32_e32 v141, 0x42800000, v141
	v_med3_f32 v132, v132, s20, v171
	v_med3_f32 v133, v133, s20, v171
	v_mul_f32_e32 v144, 0x42800000, v144
	v_mul_f32_e32 v145, 0x42800000, v145
	v_med3_f32 v140, v140, s20, v171
	v_med3_f32 v141, v141, s20, v171
	v_cvt_pk_fp8_f32 v151, v132, v133 op_sel:[0,0,1]
	v_ashrrev_i32_e32 v132, 8, v210
	v_med3_f32 v144, v144, s20, v171
	v_med3_f32 v145, v145, s20, v171
	v_cvt_pk_fp8_f32 v150, v140, v141 op_sel:[0,0,1]
	v_mad_i64_i32 v[132:133], s[26:27], s2, v132, v[130:131]
	v_lshrrev_b32_e32 v140, 3, v211
	v_cvt_pk_fp8_f32 v149, v144, v145 op_sel:[0,0,1]
	v_lshlrev_b64 v[132:133], 15, v[132:133]
	v_lshlrev_b32_e32 v138, 7, v210
	v_and_or_b32 v140, v140, s12, v208
	v_lshlrev_b32_e32 v141, 6, v211
	v_lshlrev_b32_e32 v142, 2, v211
	v_and_b32_e32 v138, 0x4000, v138
	v_mov_b32_e32 v139, v137
	v_and_or_b32 v141, v141, s13, v209
	v_lshlrev_b32_e32 v140, 10, v140
	v_and_b32_e32 v142, 32, v142
	v_lshl_add_u64 v[132:133], s[70:71], 0, v[132:133]
	v_bitop3_b32 v140, v141, v140, v142 bitop3:0xde
	v_mov_b32_e32 v141, v137
	v_lshl_add_u64 v[132:133], v[132:133], 0, v[138:139]
	v_lshl_add_u64 v[132:133], v[132:133], 0, v[140:141]
	global_store_dwordx4 v[132:133], v[148:151], off nt
	ds_read2_b32 v[148:149], v164 offset0:48 offset1:113
	ds_read2_b32 v[150:151], v164 offset0:178 offset1:243
	ds_read2_b32 v[144:145], v175 offset0:52 offset1:117
	ds_read2_b32 v[146:147], v175 offset0:182 offset1:247
	ds_read2_b32 v[140:141], v174 offset0:56 offset1:121
	ds_read2_b32 v[142:143], v174 offset0:186 offset1:251
	ds_read2_b32 v[132:133], v173 offset0:60 offset1:125
	ds_read2_b32 v[138:139], v173 offset0:190 offset1:255
	v_add_u32_e32 v210, s15, v167
	s_mov_b64 s[96:97], -1
	s_and_b64 vcc, exec, s[0:1]
	s_cbranch_vccnz .LBB0_74
	v_and_b32_e32 v211, 0x7f, v210
	s_mov_b64 s[96:97], 0

.LBB0_76:
	s_waitcnt lgkmcnt(7)
	v_mul_f32_e32 v148, 0x42800000, v148
	v_med3_f32 v212, v148, s20, v171
	v_mul_f32_e32 v148, 0x42800000, v149
	v_med3_f32 v149, v148, s20, v171
	v_mov_b32_e32 v148, v137
	v_cvt_pk_fp8_f32 v148, v212, v149
	s_waitcnt lgkmcnt(6)
	v_mul_f32_e32 v150, 0x42800000, v150
	v_mul_f32_e32 v151, 0x42800000, v151
	v_med3_f32 v150, v150, s20, v171
	v_med3_f32 v151, v151, s20, v171
	s_waitcnt lgkmcnt(1)
	v_mul_f32_e32 v132, 0x42800000, v132
	v_mul_f32_e32 v133, 0x42800000, v133
	v_cvt_pk_fp8_f32 v148, v150, v151 op_sel:[0,0,1]
	v_mul_f32_e32 v144, 0x42800000, v144
	v_mul_f32_e32 v145, 0x42800000, v145
	v_mul_f32_e32 v140, 0x42800000, v140
	v_mul_f32_e32 v141, 0x42800000, v141
	v_med3_f32 v132, v132, s20, v171
	v_med3_f32 v133, v133, s20, v171
	v_mov_b32_e32 v151, v137
	v_med3_f32 v144, v144, s20, v171
	v_med3_f32 v145, v145, s20, v171
	v_mov_b32_e32 v149, v137
	v_med3_f32 v140, v140, s20, v171
	v_med3_f32 v141, v141, s20, v171
	v_mov_b32_e32 v150, v137
	v_cvt_pk_fp8_f32 v151, v132, v133
	v_cvt_pk_fp8_f32 v149, v144, v145
	v_cvt_pk_fp8_f32 v150, v140, v141
	s_waitcnt lgkmcnt(0)
	v_mul_f32_e32 v138, 0x42800000, v138
	v_mul_f32_e32 v139, 0x42800000, v139
	v_mul_f32_e32 v146, 0x42800000, v146
	v_mul_f32_e32 v147, 0x42800000, v147
	v_mul_f32_e32 v142, 0x42800000, v142
	v_mul_f32_e32 v143, 0x42800000, v143
	v_med3_f32 v138, v138, s20, v171
	v_med3_f32 v139, v139, s20, v171
	v_ashrrev_i32_e32 v132, 8, v210
	v_med3_f32 v146, v146, s20, v171
	v_med3_f32 v147, v147, s20, v171
	v_med3_f32 v142, v142, s20, v171
	v_med3_f32 v143, v143, s20, v171
	v_cvt_pk_fp8_f32 v151, v138, v139 op_sel:[0,0,1]
	v_mad_i64_i32 v[130:131], s[0:1], s2, v132, v[130:131]
	v_lshrrev_b32_e32 v138, 3, v211
	v_cvt_pk_fp8_f32 v149, v146, v147 op_sel:[0,0,1]
	v_cvt_pk_fp8_f32 v150, v142, v143 op_sel:[0,0,1]
	v_lshlrev_b64 v[130:131], 15, v[130:131]
	v_lshlrev_b32_e32 v132, 7, v210
	v_and_or_b32 v138, v138, s12, v208
	v_lshlrev_b32_e32 v139, 6, v211
	v_lshlrev_b32_e32 v140, 2, v211
	v_and_b32_e32 v132, 0x4000, v132
	v_mov_b32_e32 v133, v137
	v_and_or_b32 v139, v139, s13, v209
	v_lshlrev_b32_e32 v138, 10, v138
	v_and_b32_e32 v140, 32, v140
	v_lshl_add_u64 v[130:131], s[70:71], 0, v[130:131]
	v_bitop3_b32 v138, v139, v138, v140 bitop3:0xde
	v_mov_b32_e32 v139, v137
	v_lshl_add_u64 v[130:131], v[130:131], 0, v[132:133]
	v_lshl_add_u64 v[130:131], v[130:131], 0, v[138:139]
	global_store_dwordx4 v[130:131], v[148:151], off nt
	s_waitcnt lgkmcnt(0)

.LBB0_135:
	s_ashr_i32 s0, s4, 31
	v_add_u32_e32 v75, s35, v168
	s_lshr_b32 s0, s0, 26
	s_add_i32 s0, s4, s0
	v_ashrrev_i32_e32 v70, 6, v75
	s_ashr_i32 s2, s0, 6
	v_ashrrev_i32_e32 v72, 8, v177
	v_ashrrev_i32_e32 v71, 31, v70
	v_mad_i64_i32 v[72:73], s[0:1], s2, v72, v[70:71]
	v_lshlrev_b64 v[76:77], 15, v[72:73]
	v_lshlrev_b32_e32 v72, 7, v177
	v_and_b32_e32 v78, 0x4000, v72
	v_lshrrev_b32_e32 v73, 3, v74
	v_bfe_u32 v72, v75, 5, 1
	v_and_or_b32 v80, v73, s12, v72
	v_lshlrev_b32_e32 v73, 1, v75
	v_lshlrev_b32_e32 v81, 6, v74
	v_and_b32_e32 v73, 62, v73
	v_lshlrev_b32_e32 v74, 2, v74
	v_mov_b32_e32 v79, v137
	v_and_or_b32 v75, v81, s13, v73
	v_lshlrev_b32_e32 v80, 10, v80
	v_and_b32_e32 v74, 32, v74
	v_lshl_add_u64 v[76:77], s[70:71], 0, v[76:77]
	v_bitop3_b32 v74, v75, v80, v74 bitop3:0xde
	v_mov_b32_e32 v75, v137
	v_lshl_add_u64 v[76:77], v[76:77], 0, v[78:79]
	v_lshl_add_u64 v[74:75], v[76:77], 0, v[74:75]
	global_store_dwordx4 v[74:75], v[66:69], off nt
	ds_read2_b32 v[66:67], v155 offset0:8 offset1:73
	ds_read2_b32 v[68:69], v155 offset0:138 offset1:203
	s_waitcnt lgkmcnt(1)
	v_cvt_pk_bf16_f32 v66, v66, v67
	s_waitcnt lgkmcnt(0)
	v_cvt_pk_bf16_f32 v67, v68, v69
	ds_read2_b32 v[68:69], v172 offset0:12 offset1:77
	ds_read2_b32 v[74:75], v172 offset0:142 offset1:207
	s_waitcnt lgkmcnt(1)
	v_cvt_pk_bf16_f32 v68, v68, v69
	s_waitcnt lgkmcnt(0)
	v_cvt_pk_bf16_f32 v69, v74, v75
	v_cndmask_b32_e64 v75, 0, 1, s[90:91]
	v_add_u32_e32 v74, s15, v156
	s_mov_b64 s[94:95], -1
	v_cmp_ne_u32_e64 s[0:1], 1, v75
	s_andn2_b64 vcc, exec, s[90:91]
	s_cbranch_vccnz .LBB0_137
	v_and_b32_e32 v75, 0x7f, v74
	s_mov_b64 s[94:95], 0

.LBB0_139:
	v_ashrrev_i32_e32 v76, 8, v74
	v_lshlrev_b32_e32 v74, 7, v74
	v_mad_i64_i32 v[76:77], s[26:27], s2, v76, v[70:71]
	v_and_b32_e32 v78, 0x4000, v74
	v_lshrrev_b32_e32 v74, 3, v75
	v_lshlrev_b64 v[76:77], 15, v[76:77]
	v_and_or_b32 v74, v74, s12, v72
	v_lshlrev_b32_e32 v80, 6, v75
	v_lshlrev_b32_e32 v75, 2, v75
	v_mov_b32_e32 v79, v137
	v_and_or_b32 v80, v80, s13, v73
	v_lshlrev_b32_e32 v74, 10, v74
	v_and_b32_e32 v75, 32, v75
	v_lshl_add_u64 v[76:77], s[70:71], 0, v[76:77]
	v_bitop3_b32 v74, v80, v74, v75 bitop3:0xde
	v_mov_b32_e32 v75, v137
	v_lshl_add_u64 v[76:77], v[76:77], 0, v[78:79]
	v_lshl_add_u64 v[74:75], v[76:77], 0, v[74:75]
	global_store_dwordx4 v[74:75], v[66:69], off nt
	ds_read2_b32 v[66:67], v155 offset0:16 offset1:81
	ds_read2_b32 v[68:69], v155 offset0:146 offset1:211
	s_waitcnt lgkmcnt(1)
	v_cvt_pk_bf16_f32 v66, v66, v67
	s_waitcnt lgkmcnt(0)
	v_cvt_pk_bf16_f32 v67, v68, v69
	ds_read2_b32 v[68:69], v172 offset0:20 offset1:85
	ds_read2_b32 v[74:75], v172 offset0:150 offset1:215
	s_waitcnt lgkmcnt(1)
	v_cvt_pk_bf16_f32 v68, v68, v69
	s_waitcnt lgkmcnt(0)
	v_cvt_pk_bf16_f32 v69, v74, v75
	v_add_u32_e32 v74, s15, v157
	s_mov_b64 s[94:95], -1
	s_and_b64 vcc, exec, s[0:1]
	s_cbranch_vccnz .LBB0_141
	v_and_b32_e32 v75, 0x7f, v74
	s_mov_b64 s[94:95], 0

.LBB0_143:
	v_ashrrev_i32_e32 v76, 8, v74
	v_lshlrev_b32_e32 v74, 7, v74
	v_mad_i64_i32 v[76:77], s[26:27], s2, v76, v[70:71]
	v_and_b32_e32 v78, 0x4000, v74
	v_lshrrev_b32_e32 v74, 3, v75
	v_lshlrev_b64 v[76:77], 15, v[76:77]
	v_and_or_b32 v74, v74, s12, v72
	v_lshlrev_b32_e32 v80, 6, v75
	v_lshlrev_b32_e32 v75, 2, v75
	v_mov_b32_e32 v79, v137
	v_and_or_b32 v80, v80, s13, v73
	v_lshlrev_b32_e32 v74, 10, v74
	v_and_b32_e32 v75, 32, v75
	v_lshl_add_u64 v[76:77], s[70:71], 0, v[76:77]
	v_bitop3_b32 v74, v80, v74, v75 bitop3:0xde
	v_mov_b32_e32 v75, v137
	v_lshl_add_u64 v[76:77], v[76:77], 0, v[78:79]
	v_lshl_add_u64 v[74:75], v[76:77], 0, v[74:75]
	global_store_dwordx4 v[74:75], v[66:69], off nt
	ds_read2_b32 v[66:67], v155 offset0:24 offset1:89
	ds_read2_b32 v[68:69], v155 offset0:154 offset1:219
	s_waitcnt lgkmcnt(1)
	v_cvt_pk_bf16_f32 v66, v66, v67
	s_waitcnt lgkmcnt(0)
	v_cvt_pk_bf16_f32 v67, v68, v69
	ds_read2_b32 v[68:69], v172 offset0:28 offset1:93
	ds_read2_b32 v[74:75], v172 offset0:158 offset1:223
	s_waitcnt lgkmcnt(1)
	v_cvt_pk_bf16_f32 v68, v68, v69
	s_waitcnt lgkmcnt(0)
	v_cvt_pk_bf16_f32 v69, v74, v75
	v_add_u32_e32 v74, s15, v158
	s_mov_b64 s[94:95], -1
	s_and_b64 vcc, exec, s[0:1]
	s_cbranch_vccnz .LBB0_145
	v_and_b32_e32 v75, 0x7f, v74
	s_mov_b64 s[94:95], 0

.LBB0_147:
	v_ashrrev_i32_e32 v76, 8, v74
	v_lshlrev_b32_e32 v74, 7, v74
	v_mad_i64_i32 v[76:77], s[26:27], s2, v76, v[70:71]
	v_and_b32_e32 v78, 0x4000, v74
	v_lshrrev_b32_e32 v74, 3, v75
	v_lshlrev_b64 v[76:77], 15, v[76:77]
	v_and_or_b32 v74, v74, s12, v72
	v_lshlrev_b32_e32 v80, 6, v75
	v_lshlrev_b32_e32 v75, 2, v75
	v_mov_b32_e32 v79, v137
	v_and_or_b32 v80, v80, s13, v73
	v_lshlrev_b32_e32 v74, 10, v74
	v_and_b32_e32 v75, 32, v75
	v_lshl_add_u64 v[76:77], s[70:71], 0, v[76:77]
	v_bitop3_b32 v74, v80, v74, v75 bitop3:0xde
	v_mov_b32_e32 v75, v137
	v_lshl_add_u64 v[76:77], v[76:77], 0, v[78:79]
	v_lshl_add_u64 v[74:75], v[76:77], 0, v[74:75]
	global_store_dwordx4 v[74:75], v[66:69], off nt
	ds_read2_b32 v[66:67], v155 offset0:32 offset1:97
	ds_read2_b32 v[68:69], v155 offset0:162 offset1:227
	s_waitcnt lgkmcnt(1)
	v_cvt_pk_bf16_f32 v66, v66, v67
	s_waitcnt lgkmcnt(0)
	v_cvt_pk_bf16_f32 v67, v68, v69
	ds_read2_b32 v[68:69], v172 offset0:36 offset1:101
	ds_read2_b32 v[74:75], v172 offset0:166 offset1:231
	s_waitcnt lgkmcnt(1)
	v_cvt_pk_bf16_f32 v68, v68, v69
	s_waitcnt lgkmcnt(0)
	v_cvt_pk_bf16_f32 v69, v74, v75
	v_add_u32_e32 v74, s15, v159
	s_mov_b64 s[94:95], -1
	s_and_b64 vcc, exec, s[0:1]
	s_cbranch_vccnz .LBB0_149
	v_and_b32_e32 v75, 0x7f, v74
	s_mov_b64 s[94:95], 0

.LBB0_151:
	v_ashrrev_i32_e32 v76, 8, v74
	v_lshlrev_b32_e32 v74, 7, v74
	v_mad_i64_i32 v[76:77], s[26:27], s2, v76, v[70:71]
	v_and_b32_e32 v78, 0x4000, v74
	v_lshrrev_b32_e32 v74, 3, v75
	v_lshlrev_b64 v[76:77], 15, v[76:77]
	v_and_or_b32 v74, v74, s12, v72
	v_lshlrev_b32_e32 v80, 6, v75
	v_lshlrev_b32_e32 v75, 2, v75
	v_mov_b32_e32 v79, v137
	v_and_or_b32 v80, v80, s13, v73
	v_lshlrev_b32_e32 v74, 10, v74
	v_and_b32_e32 v75, 32, v75
	v_lshl_add_u64 v[76:77], s[70:71], 0, v[76:77]
	v_bitop3_b32 v74, v80, v74, v75 bitop3:0xde
	v_mov_b32_e32 v75, v137
	v_lshl_add_u64 v[76:77], v[76:77], 0, v[78:79]
	v_lshl_add_u64 v[74:75], v[76:77], 0, v[74:75]
	global_store_dwordx4 v[74:75], v[66:69], off nt
	ds_read2_b32 v[66:67], v155 offset0:40 offset1:105
	ds_read2_b32 v[68:69], v155 offset0:170 offset1:235
	s_waitcnt lgkmcnt(1)
	v_cvt_pk_bf16_f32 v66, v66, v67
	s_waitcnt lgkmcnt(0)
	v_cvt_pk_bf16_f32 v67, v68, v69
	ds_read2_b32 v[68:69], v172 offset0:44 offset1:109
	ds_read2_b32 v[74:75], v172 offset0:174 offset1:239
	s_waitcnt lgkmcnt(1)
	v_cvt_pk_bf16_f32 v68, v68, v69
	s_waitcnt lgkmcnt(0)
	v_cvt_pk_bf16_f32 v69, v74, v75
	v_add_u32_e32 v74, s15, v160
	s_mov_b64 s[94:95], -1
	s_and_b64 vcc, exec, s[0:1]
	s_cbranch_vccnz .LBB0_153
	v_and_b32_e32 v75, 0x7f, v74
	s_mov_b64 s[94:95], 0

.LBB0_155:
	v_ashrrev_i32_e32 v76, 8, v74
	v_lshlrev_b32_e32 v74, 7, v74
	v_mad_i64_i32 v[76:77], s[26:27], s2, v76, v[70:71]
	v_and_b32_e32 v78, 0x4000, v74
	v_lshrrev_b32_e32 v74, 3, v75
	v_lshlrev_b64 v[76:77], 15, v[76:77]
	v_and_or_b32 v74, v74, s12, v72
	v_lshlrev_b32_e32 v80, 6, v75
	v_lshlrev_b32_e32 v75, 2, v75
	v_mov_b32_e32 v79, v137
	v_and_or_b32 v80, v80, s13, v73
	v_lshlrev_b32_e32 v74, 10, v74
	v_and_b32_e32 v75, 32, v75
	v_lshl_add_u64 v[76:77], s[70:71], 0, v[76:77]
	v_bitop3_b32 v74, v80, v74, v75 bitop3:0xde
	v_mov_b32_e32 v75, v137
	v_lshl_add_u64 v[76:77], v[76:77], 0, v[78:79]
	v_lshl_add_u64 v[74:75], v[76:77], 0, v[74:75]
	global_store_dwordx4 v[74:75], v[66:69], off nt
	ds_read2_b32 v[66:67], v155 offset0:48 offset1:113
	ds_read2_b32 v[68:69], v155 offset0:178 offset1:243
	s_waitcnt lgkmcnt(1)
	v_cvt_pk_bf16_f32 v66, v66, v67
	s_waitcnt lgkmcnt(0)
	v_cvt_pk_bf16_f32 v67, v68, v69
	ds_read2_b32 v[68:69], v172 offset0:52 offset1:117
	ds_read2_b32 v[74:75], v172 offset0:182 offset1:247
	s_waitcnt lgkmcnt(1)
	v_cvt_pk_bf16_f32 v68, v68, v69
	s_waitcnt lgkmcnt(0)
	v_cvt_pk_bf16_f32 v69, v74, v75
	v_add_u32_e32 v74, s15, v161
	s_mov_b64 s[94:95], -1
	s_and_b64 vcc, exec, s[0:1]
	s_cbranch_vccnz .LBB0_157
	v_and_b32_e32 v75, 0x7f, v74
	s_mov_b64 s[94:95], 0

.LBB0_159:
	v_ashrrev_i32_e32 v76, 8, v74
	v_lshlrev_b32_e32 v74, 7, v74
	v_mad_i64_i32 v[76:77], s[26:27], s2, v76, v[70:71]
	v_and_b32_e32 v78, 0x4000, v74
	v_lshrrev_b32_e32 v74, 3, v75
	v_lshlrev_b64 v[76:77], 15, v[76:77]
	v_and_or_b32 v74, v74, s12, v72
	v_lshlrev_b32_e32 v80, 6, v75
	v_lshlrev_b32_e32 v75, 2, v75
	v_mov_b32_e32 v79, v137
	v_and_or_b32 v80, v80, s13, v73
	v_lshlrev_b32_e32 v74, 10, v74
	v_and_b32_e32 v75, 32, v75
	v_lshl_add_u64 v[76:77], s[70:71], 0, v[76:77]
	v_bitop3_b32 v74, v80, v74, v75 bitop3:0xde
	v_mov_b32_e32 v75, v137
	v_lshl_add_u64 v[76:77], v[76:77], 0, v[78:79]
	v_lshl_add_u64 v[74:75], v[76:77], 0, v[74:75]
	global_store_dwordx4 v[74:75], v[66:69], off nt
	ds_read2_b32 v[66:67], v155 offset0:56 offset1:121
	ds_read2_b32 v[68:69], v155 offset0:186 offset1:251
	s_waitcnt lgkmcnt(1)
	v_cvt_pk_bf16_f32 v66, v66, v67
	s_waitcnt lgkmcnt(0)
	v_cvt_pk_bf16_f32 v67, v68, v69
	ds_read2_b32 v[68:69], v172 offset0:60 offset1:125
	ds_read2_b32 v[74:75], v172 offset0:190 offset1:255
	s_waitcnt lgkmcnt(1)
	v_cvt_pk_bf16_f32 v68, v68, v69
	s_waitcnt lgkmcnt(0)
	v_cvt_pk_bf16_f32 v69, v74, v75
	v_add_u32_e32 v74, s15, v162
	s_mov_b64 s[94:95], -1
	s_and_b64 vcc, exec, s[0:1]
	s_cbranch_vccnz .LBB0_161
	v_and_b32_e32 v75, 0x7f, v74
	s_mov_b64 s[94:95], 0

.LBB0_163:
	v_ashrrev_i32_e32 v76, 8, v74
	v_lshlrev_b32_e32 v74, 7, v74
	v_mad_i64_i32 v[70:71], s[0:1], s2, v76, v[70:71]
	v_and_b32_e32 v76, 0x4000, v74
	v_lshrrev_b32_e32 v74, 3, v75
	v_and_or_b32 v72, v74, s12, v72
	v_lshlrev_b32_e32 v74, 6, v75
	v_lshlrev_b64 v[70:71], 15, v[70:71]
	v_and_or_b32 v73, v74, s13, v73
	v_lshlrev_b32_e32 v74, 2, v75
	v_mov_b32_e32 v77, v137
	v_lshlrev_b32_e32 v72, 10, v72
	v_and_b32_e32 v74, 32, v74
	v_lshl_add_u64 v[70:71], s[70:71], 0, v[70:71]
	v_bitop3_b32 v72, v73, v72, v74 bitop3:0xde
	v_mov_b32_e32 v73, v137
	v_lshl_add_u64 v[70:71], v[70:71], 0, v[76:77]
	v_lshl_add_u64 v[70:71], v[70:71], 0, v[72:73]
	global_store_dwordx4 v[70:71], v[66:69], off nt
	s_waitcnt lgkmcnt(0)
	s_mov_b64 s[0:1], 0

.LBB0_169:
	s_waitcnt lgkmcnt(7)
	v_mul_f32_e32 v80, 0x42800000, v80
	v_mul_f32_e32 v81, 0x42800000, v81
	s_waitcnt lgkmcnt(6)
	v_mul_f32_e32 v83, 0x42800000, v78
	v_med3_f32 v80, v80, s20, v171
	v_med3_f32 v81, v81, s20, v171
	v_mov_b32_e32 v78, v137
	v_cvt_pk_fp8_f32 v78, v80, v81
	s_waitcnt lgkmcnt(1)
	v_mul_f32_e32 v68, 0x42800000, v68
	v_mul_f32_e32 v69, 0x42800000, v69
	v_mul_f32_e32 v79, 0x42800000, v79
	v_med3_f32 v68, v68, s20, v171
	v_med3_f32 v69, v69, s20, v171
	v_mov_b32_e32 v81, v137
	v_med3_f32 v80, v83, s20, v171
	v_med3_f32 v79, v79, s20, v171
	v_mul_f32_e32 v76, 0x42800000, v76
	v_mul_f32_e32 v77, 0x42800000, v77
	v_cvt_pk_fp8_f32 v81, v68, v69
	v_cvt_pk_fp8_f32 v78, v80, v79 op_sel:[0,0,1]
	v_med3_f32 v76, v76, s20, v171
	v_med3_f32 v77, v77, s20, v171
	v_mov_b32_e32 v79, v137
	v_mul_f32_e32 v72, 0x42800000, v72
	v_mul_f32_e32 v73, 0x42800000, v73
	v_cvt_pk_fp8_f32 v79, v76, v77
	v_med3_f32 v72, v72, s20, v171
	v_med3_f32 v73, v73, s20, v171
	v_mov_b32_e32 v80, v137
	s_waitcnt lgkmcnt(0)
	v_mul_f32_e32 v66, 0x42800000, v66
	v_mul_f32_e32 v67, 0x42800000, v67
	s_ashr_i32 s0, s4, 31
	v_cvt_pk_fp8_f32 v80, v72, v73
	v_med3_f32 v66, v66, s20, v171
	v_med3_f32 v67, v67, s20, v171
	v_add_u32_e32 v72, s35, v169
	s_lshr_b32 s0, s0, 25
	v_mul_f32_e32 v74, 0x42800000, v74
	v_mul_f32_e32 v75, 0x42800000, v75
	v_cvt_pk_fp8_f32 v81, v66, v67 op_sel:[0,0,1]
	s_add_i32 s0, s4, s0
	v_ashrrev_i32_e32 v66, 7, v72
	v_med3_f32 v74, v74, s20, v171
	v_med3_f32 v75, v75, s20, v171
	v_mul_f32_e32 v70, 0x42800000, v70
	v_mul_f32_e32 v71, 0x42800000, v71
	s_ashr_i32 s2, s0, 7
	v_ashrrev_i32_e32 v68, 8, v176
	v_ashrrev_i32_e32 v67, 31, v66
	v_cvt_pk_fp8_f32 v79, v74, v75 op_sel:[0,0,1]
	v_med3_f32 v70, v70, s20, v171
	v_med3_f32 v71, v71, s20, v171
	v_mad_i64_i32 v[68:69], s[0:1], s2, v68, v[66:67]
	v_lshrrev_b32_e32 v73, 3, v82
	v_bfe_u32 v84, v72, 6, 1
	v_lshlrev_b32_e32 v74, 6, v82
	v_and_b32_e32 v85, 62, v72
	v_cvt_pk_fp8_f32 v80, v70, v71 op_sel:[0,0,1]
	v_lshlrev_b64 v[68:69], 15, v[68:69]
	v_lshlrev_b32_e32 v70, 7, v176
	v_and_or_b32 v73, v73, s12, v84
	v_and_or_b32 v72, v74, s13, v85
	v_lshlrev_b32_e32 v74, 2, v82
	v_and_b32_e32 v70, 0x4000, v70
	v_mov_b32_e32 v71, v137
	v_lshlrev_b32_e32 v73, 10, v73
	v_and_b32_e32 v74, 32, v74
	v_lshl_add_u64 v[68:69], s[70:71], 0, v[68:69]
	v_bitop3_b32 v72, v72, v73, v74 bitop3:0xde
	v_mov_b32_e32 v73, v137
	v_lshl_add_u64 v[68:69], v[68:69], 0, v[70:71]
	v_lshl_add_u64 v[68:69], v[68:69], 0, v[72:73]
	global_store_dwordx4 v[68:69], v[78:81], off nt
	ds_read2_b32 v[82:83], v164 offset0:16 offset1:81
	ds_read2_b32 v[80:81], v164 offset0:146 offset1:211
	ds_read2_b32 v[78:79], v175 offset0:20 offset1:85
	ds_read2_b32 v[76:77], v175 offset0:150 offset1:215
	ds_read2_b32 v[74:75], v174 offset0:24 offset1:89
	ds_read2_b32 v[72:73], v174 offset0:154 offset1:219
	ds_read2_b32 v[70:71], v173 offset0:28 offset1:93
	ds_read2_b32 v[68:69], v173 offset0:158 offset1:223
	v_cndmask_b32_e64 v87, 0, 1, s[90:91]
	v_add_u32_e32 v86, s15, v165
	v_cmp_ne_u32_e64 s[0:1], 1, v87
	s_andn2_b64 vcc, exec, s[90:91]
	s_mov_b64 s[90:91], -1
	s_cbranch_vccnz .LBB0_171
	v_and_b32_e32 v87, 0x7f, v86
	s_mov_b64 s[90:91], 0

.LBB0_173:
	s_waitcnt lgkmcnt(7)
	v_mul_f32_e32 v82, 0x42800000, v82
	v_mul_f32_e32 v83, 0x42800000, v83
	s_waitcnt lgkmcnt(6)
	v_mul_f32_e32 v88, 0x42800000, v80
	v_med3_f32 v82, v82, s20, v171
	v_med3_f32 v83, v83, s20, v171
	v_mov_b32_e32 v80, v137
	v_cvt_pk_fp8_f32 v80, v82, v83
	v_mul_f32_e32 v81, 0x42800000, v81
	s_waitcnt lgkmcnt(1)
	v_mul_f32_e32 v70, 0x42800000, v70
	v_mul_f32_e32 v71, 0x42800000, v71
	v_med3_f32 v82, v88, s20, v171
	v_med3_f32 v81, v81, s20, v171
	v_mul_f32_e32 v74, 0x42800000, v74
	v_mul_f32_e32 v75, 0x42800000, v75
	v_med3_f32 v70, v70, s20, v171
	v_med3_f32 v71, v71, s20, v171
	v_mov_b32_e32 v83, v137
	v_cvt_pk_fp8_f32 v80, v82, v81 op_sel:[0,0,1]
	v_mul_f32_e32 v78, 0x42800000, v78
	v_mul_f32_e32 v79, 0x42800000, v79
	v_med3_f32 v74, v74, s20, v171
	v_med3_f32 v75, v75, s20, v171
	v_mov_b32_e32 v82, v137
	v_cvt_pk_fp8_f32 v83, v70, v71
	v_med3_f32 v78, v78, s20, v171
	v_med3_f32 v79, v79, s20, v171
	v_mov_b32_e32 v81, v137
	v_cvt_pk_fp8_f32 v82, v74, v75
	v_cvt_pk_fp8_f32 v81, v78, v79
	s_waitcnt lgkmcnt(0)
	v_mul_f32_e32 v68, 0x42800000, v68
	v_mul_f32_e32 v69, 0x42800000, v69
	v_mul_f32_e32 v72, 0x42800000, v72
	v_mul_f32_e32 v73, 0x42800000, v73
	v_med3_f32 v68, v68, s20, v171
	v_med3_f32 v69, v69, s20, v171
	v_mul_f32_e32 v76, 0x42800000, v76
	v_mul_f32_e32 v77, 0x42800000, v77
	v_med3_f32 v72, v72, s20, v171
	v_med3_f32 v73, v73, s20, v171
	v_cvt_pk_fp8_f32 v83, v68, v69 op_sel:[0,0,1]
	v_ashrrev_i32_e32 v68, 8, v86
	v_med3_f32 v76, v76, s20, v171
	v_med3_f32 v77, v77, s20, v171
	v_cvt_pk_fp8_f32 v82, v72, v73 op_sel:[0,0,1]
	v_mad_i64_i32 v[68:69], s[26:27], s2, v68, v[66:67]
	v_lshrrev_b32_e32 v72, 3, v87
	v_cvt_pk_fp8_f32 v81, v76, v77 op_sel:[0,0,1]
	v_lshlrev_b64 v[68:69], 15, v[68:69]
	v_lshlrev_b32_e32 v70, 7, v86
	v_and_or_b32 v72, v72, s12, v84
	v_lshlrev_b32_e32 v73, 6, v87
	v_lshlrev_b32_e32 v74, 2, v87
	v_and_b32_e32 v70, 0x4000, v70
	v_mov_b32_e32 v71, v137
	v_and_or_b32 v73, v73, s13, v85
	v_lshlrev_b32_e32 v72, 10, v72
	v_and_b32_e32 v74, 32, v74
	v_lshl_add_u64 v[68:69], s[70:71], 0, v[68:69]
	v_bitop3_b32 v72, v73, v72, v74 bitop3:0xde
	v_mov_b32_e32 v73, v137
	v_lshl_add_u64 v[68:69], v[68:69], 0, v[70:71]
	v_lshl_add_u64 v[68:69], v[68:69], 0, v[72:73]
	global_store_dwordx4 v[68:69], v[80:83], off nt
	ds_read2_b32 v[82:83], v164 offset0:32 offset1:97
	ds_read2_b32 v[80:81], v164 offset0:162 offset1:227
	ds_read2_b32 v[78:79], v175 offset0:36 offset1:101
	ds_read2_b32 v[76:77], v175 offset0:166 offset1:231
	ds_read2_b32 v[74:75], v174 offset0:40 offset1:105
	ds_read2_b32 v[72:73], v174 offset0:170 offset1:235
	ds_read2_b32 v[70:71], v173 offset0:44 offset1:109
	ds_read2_b32 v[68:69], v173 offset0:174 offset1:239
	v_add_u32_e32 v86, s15, v166
	s_mov_b64 s[90:91], -1
	s_and_b64 vcc, exec, s[0:1]
	s_cbranch_vccnz .LBB0_175
	v_and_b32_e32 v87, 0x7f, v86
	s_mov_b64 s[90:91], 0

.LBB0_177:
	s_waitcnt lgkmcnt(7)
	v_mul_f32_e32 v82, 0x42800000, v82
	v_mul_f32_e32 v83, 0x42800000, v83
	s_waitcnt lgkmcnt(6)
	v_mul_f32_e32 v88, 0x42800000, v80
	v_med3_f32 v82, v82, s20, v171
	v_med3_f32 v83, v83, s20, v171
	v_mov_b32_e32 v80, v137
	v_cvt_pk_fp8_f32 v80, v82, v83
	v_mul_f32_e32 v81, 0x42800000, v81
	s_waitcnt lgkmcnt(1)
	v_mul_f32_e32 v70, 0x42800000, v70
	v_mul_f32_e32 v71, 0x42800000, v71
	v_med3_f32 v82, v88, s20, v171
	v_med3_f32 v81, v81, s20, v171
	v_mul_f32_e32 v74, 0x42800000, v74
	v_mul_f32_e32 v75, 0x42800000, v75
	v_med3_f32 v70, v70, s20, v171
	v_med3_f32 v71, v71, s20, v171
	v_mov_b32_e32 v83, v137
	v_cvt_pk_fp8_f32 v80, v82, v81 op_sel:[0,0,1]
	v_mul_f32_e32 v78, 0x42800000, v78
	v_mul_f32_e32 v79, 0x42800000, v79
	v_med3_f32 v74, v74, s20, v171
	v_med3_f32 v75, v75, s20, v171
	v_mov_b32_e32 v82, v137
	v_cvt_pk_fp8_f32 v83, v70, v71
	v_med3_f32 v78, v78, s20, v171
	v_med3_f32 v79, v79, s20, v171
	v_mov_b32_e32 v81, v137
	v_cvt_pk_fp8_f32 v82, v74, v75
	v_cvt_pk_fp8_f32 v81, v78, v79
	s_waitcnt lgkmcnt(0)
	v_mul_f32_e32 v68, 0x42800000, v68
	v_mul_f32_e32 v69, 0x42800000, v69
	v_mul_f32_e32 v72, 0x42800000, v72
	v_mul_f32_e32 v73, 0x42800000, v73
	v_med3_f32 v68, v68, s20, v171
	v_med3_f32 v69, v69, s20, v171
	v_mul_f32_e32 v76, 0x42800000, v76
	v_mul_f32_e32 v77, 0x42800000, v77
	v_med3_f32 v72, v72, s20, v171
	v_med3_f32 v73, v73, s20, v171
	v_cvt_pk_fp8_f32 v83, v68, v69 op_sel:[0,0,1]
	v_ashrrev_i32_e32 v68, 8, v86
	v_med3_f32 v76, v76, s20, v171
	v_med3_f32 v77, v77, s20, v171
	v_cvt_pk_fp8_f32 v82, v72, v73 op_sel:[0,0,1]
	v_mad_i64_i32 v[68:69], s[26:27], s2, v68, v[66:67]
	v_lshrrev_b32_e32 v72, 3, v87
	v_cvt_pk_fp8_f32 v81, v76, v77 op_sel:[0,0,1]
	v_lshlrev_b64 v[68:69], 15, v[68:69]
	v_lshlrev_b32_e32 v70, 7, v86
	v_and_or_b32 v72, v72, s12, v84
	v_lshlrev_b32_e32 v73, 6, v87
	v_lshlrev_b32_e32 v74, 2, v87
	v_and_b32_e32 v70, 0x4000, v70
	v_mov_b32_e32 v71, v137
	v_and_or_b32 v73, v73, s13, v85
	v_lshlrev_b32_e32 v72, 10, v72
	v_and_b32_e32 v74, 32, v74
	v_lshl_add_u64 v[68:69], s[70:71], 0, v[68:69]
	v_bitop3_b32 v72, v73, v72, v74 bitop3:0xde
	v_mov_b32_e32 v73, v137
	v_lshl_add_u64 v[68:69], v[68:69], 0, v[70:71]
	v_lshl_add_u64 v[68:69], v[68:69], 0, v[72:73]
	global_store_dwordx4 v[68:69], v[80:83], off nt
	ds_read2_b32 v[80:81], v164 offset0:48 offset1:113
	ds_read2_b32 v[82:83], v164 offset0:178 offset1:243
	ds_read2_b32 v[76:77], v175 offset0:52 offset1:117
	ds_read2_b32 v[78:79], v175 offset0:182 offset1:247
	ds_read2_b32 v[72:73], v174 offset0:56 offset1:121
	ds_read2_b32 v[74:75], v174 offset0:186 offset1:251
	ds_read2_b32 v[68:69], v173 offset0:60 offset1:125
	ds_read2_b32 v[70:71], v173 offset0:190 offset1:255
	v_add_u32_e32 v86, s15, v167
	s_mov_b64 s[90:91], -1
	s_and_b64 vcc, exec, s[0:1]
	s_cbranch_vccnz .LBB0_179
	v_and_b32_e32 v87, 0x7f, v86
	s_mov_b64 s[90:91], 0
